# v44 + thin2->gate/up GEMM grid barrier replaced by batch-group hand-off plus a chip-wide attention-done guard (R1 reuse), global kept for the last mixer
# baseline (speedup 1.0000x reference)
; __device__ __forceinline__ unsigned xb_ld(unsigned* p)              { return __hip_atomic_load(p, __ATOMIC_RELAXED, __HIP_MEMORY_SCOPE_AGENT); }
; __device__ __forceinline__ unsigned xb_add(unsigned* p, unsigned v) { return __hip_atomic_fetch_add(p, v, __ATOMIC_RELAXED, __HIP_MEMORY_SCOPE_AGENT); }
; #define XB_SPIN(cond, bar) do { unsigned _sp = 0; while (cond) { __builtin_amdgcn_s_sleep(1); \
;     if ((++_sp & 255u) == 0u) { if (xb_ld(&(bar)[XB_TMO])) break; if (_sp > XB_SPIN_CAP) { atomicAdd(&(bar)[XB_TMO], 1u); break; } } } } while (0)
; __device__ __forceinline__ void xcd_barrier(const XcdBarrier& b) {
;     asm volatile("s_waitcnt vmcnt(0)" ::: "memory");
;     __syncthreads();
;     if (threadIdx.x == 0) {
;         unsigned* bar = b.bar;
;         __builtin_amdgcn_s_waitcnt(0);
;         unsigned nloc = b.st[0], nx = b.st[1];
;         if (nloc == 0u) { xcd_barrier_complete(bar, b.x, nloc, nx); b.st[0] = nloc; b.st[1] = nx; }
;         const unsigned old = xb_add(&bar[XB_XSUB(b.x)], 1u);
;         const unsigned gen = old / nloc;
;         if (old + 1u == (gen + 1u) * nloc) {
;             __builtin_amdgcn_fence(__ATOMIC_RELEASE, "agent");
;             asm volatile("s_waitcnt vmcnt(0)" ::: "memory");
;             const unsigned og = xb_add(&bar[XB_TOP], 1u);
;             const unsigned tg = og / nx;
;             if (og + 1u == (tg + 1u) * nx) xb_add(&bar[XB_TOPGEN], 1u);
;             else XB_SPIN(xb_ld(&bar[XB_TOPGEN]) == tg, bar);
;             __builtin_amdgcn_fence(__ATOMIC_ACQUIRE, "agent");
;             xb_add(&bar[XB_XGEN(b.x)], 1u);
;             asm volatile("s_waitcnt vmcnt(0)" ::: "memory");
;         } else {
;             XB_SPIN(xb_ld(&bar[XB_XGEN(b.x)]) == gen, bar);
;             __builtin_amdgcn_fence(__ATOMIC_ACQUIRE, "agent");
;             asm volatile("s_waitcnt vmcnt(0)" ::: "memory");
;         }
;     }
;     __syncthreads();
; }
.LBB0_1027:
	v_readlane_b32 s0, v253, 42
	v_readlane_b32 s4, v253, 32
	s_add_i32 s0, s0, 5
	v_readlane_b32 s7, v253, 35
	s_cmp_ge_i32 s0, s7
	v_readlane_b32 s5, v253, 33
	v_readlane_b32 s6, v253, 34
	s_cbranch_scc1 .LBB0_1073
	v_readlane_b32 s38, v253, 36
	v_readlane_b32 s39, v253, 37
	s_mov_b32 s1, s76
	s_waitcnt vmcnt(0)
	s_waitcnt vmcnt(0)
	s_barrier
	s_mov_b64 s[40:41], exec
	v_readlane_b32 s4, v253, 53
	v_readlane_b32 s5, v253, 54
	s_and_b64 s[4:5], s[40:41], s[4:5]
	s_mov_b64 exec, s[4:5]
	s_cbranch_execz .LBB0_1072
	v_readlane_b32 s10, v253, 36
	v_readlane_b32 s11, v253, 37
	s_nop 3
	s_add_u32 s12, s10, 0xb000
	s_addc_u32 s13, s11, 0
	s_and_b32 s15, s88, 7
	s_lshl_b32 s15, s15, 8
	v_mov_b32_e32 v2, s15
	v_mov_b32_e32 v5, 1
	global_atomic_add v2, v5, s[12:13]
	v_readlane_b32 s10, v253, 36
	v_readlane_b32 s11, v253, 37
	v_readlane_b32 s14, v253, 55
	s_nop 3
	s_add_u32 s12, s10, 0x8000
	s_addc_u32 s13, s11, 0
	s_and_b32 s15, s88, 7
	s_lshl_b32 s15, s15, 8
	s_lshr_b32 s14, s14, 2
	s_add_i32 s14, s14, 1
	s_lshl_b32 s14, s14, 5
	v_mov_b32_e32 v2, s15
	v_mov_b32_e32 v5, 1
	global_atomic_add v2, v5, s[12:13]
	s_mov_b32 s18, 0

; __device__ __forceinline__ unsigned xb_ld(unsigned* p)              { return __hip_atomic_load(p, __ATOMIC_RELAXED, __HIP_MEMORY_SCOPE_AGENT); }
; __device__ __forceinline__ unsigned xb_add(unsigned* p, unsigned v) { return __hip_atomic_fetch_add(p, v, __ATOMIC_RELAXED, __HIP_MEMORY_SCOPE_AGENT); }
; #define XB_SPIN(cond, bar) do { unsigned _sp = 0; while (cond) { __builtin_amdgcn_s_sleep(1); \
;     if ((++_sp & 255u) == 0u) { if (xb_ld(&(bar)[XB_TMO])) break; if (_sp > XB_SPIN_CAP) { atomicAdd(&(bar)[XB_TMO], 1u); break; } } } } while (0)
; __device__ __forceinline__ void xcd_barrier(const XcdBarrier& b) {
;     asm volatile("s_waitcnt vmcnt(0)" ::: "memory");
;     __syncthreads();
;     if (threadIdx.x == 0) {
;         unsigned* bar = b.bar;
;         __builtin_amdgcn_s_waitcnt(0);
;         unsigned nloc = b.st[0], nx = b.st[1];
;         if (nloc == 0u) { xcd_barrier_complete(bar, b.x, nloc, nx); b.st[0] = nloc; b.st[1] = nx; }
;         const unsigned old = xb_add(&bar[XB_XSUB(b.x)], 1u);
;         const unsigned gen = old / nloc;
;         if (old + 1u == (gen + 1u) * nloc) {
;             __builtin_amdgcn_fence(__ATOMIC_RELEASE, "agent");
;             asm volatile("s_waitcnt vmcnt(0)" ::: "memory");
;             const unsigned og = xb_add(&bar[XB_TOP], 1u);
;             const unsigned tg = og / nx;
;             if (og + 1u == (tg + 1u) * nx) xb_add(&bar[XB_TOPGEN], 1u);
;             else XB_SPIN(xb_ld(&bar[XB_TOPGEN]) == tg, bar);
;             __builtin_amdgcn_fence(__ATOMIC_ACQUIRE, "agent");
;             xb_add(&bar[XB_XGEN(b.x)], 1u);
;             asm volatile("s_waitcnt vmcnt(0)" ::: "memory");
;         } else {
;             XB_SPIN(xb_ld(&bar[XB_XGEN(b.x)]) == gen, bar);
;             __builtin_amdgcn_fence(__ATOMIC_ACQUIRE, "agent");
;             asm volatile("s_waitcnt vmcnt(0)" ::: "memory");
;         }
;     }
;     __syncthreads();
; }
.LBB0_1627:
	v_readlane_b32 s0, v253, 42
	v_readlane_b32 s4, v253, 32
	s_add_i32 s0, s0, 7
	v_readlane_b32 s7, v253, 35
	s_cmp_ge_i32 s0, s7
	v_readlane_b32 s5, v253, 33
	v_readlane_b32 s6, v253, 34
	s_cbranch_scc1 .LBB0_1673
	v_readlane_b32 s34, v253, 36
	v_readlane_b32 s35, v253, 37
	s_mov_b32 s1, s76
	s_waitcnt vmcnt(0)
	s_waitcnt vmcnt(0) lgkmcnt(0)
	s_barrier
	s_mov_b64 s[36:37], exec
	v_readlane_b32 s2, v253, 53
	v_readlane_b32 s3, v253, 54
	s_and_b64 s[2:3], s[36:37], s[2:3]
	s_mov_b64 exec, s[2:3]
	s_cbranch_execz .LBB0_1672
	v_readlane_b32 s10, v253, 36
	v_readlane_b32 s11, v253, 37
	s_nop 3
	s_add_u32 s12, s10, 0xb000
	s_addc_u32 s13, s11, 0
	s_and_b32 s15, s88, 7
	s_lshl_b32 s15, s15, 8
	v_mov_b32_e32 v2, s15
	v_mov_b32_e32 v5, 1
	global_atomic_add v2, v5, s[12:13]
	v_readlane_b32 s10, v253, 36
	v_readlane_b32 s11, v253, 37
	v_readlane_b32 s14, v253, 55
	s_nop 3
	s_add_u32 s12, s10, 0x8800
	s_addc_u32 s13, s11, 0
	s_and_b32 s15, s88, 7
	s_lshl_b32 s15, s15, 8
	s_lshr_b32 s14, s14, 2
	s_add_i32 s14, s14, 1
	s_lshl_b32 s14, s14, 5
	v_mov_b32_e32 v2, s15
	v_mov_b32_e32 v5, 1
	global_atomic_add v2, v5, s[12:13]
	s_mov_b32 s18, 0

; __device__ __forceinline__ unsigned xb_ld(unsigned* p)              { return __hip_atomic_load(p, __ATOMIC_RELAXED, __HIP_MEMORY_SCOPE_AGENT); }
; __device__ __forceinline__ unsigned xb_add(unsigned* p, unsigned v) { return __hip_atomic_fetch_add(p, v, __ATOMIC_RELAXED, __HIP_MEMORY_SCOPE_AGENT); }
; #define XB_SPIN(cond, bar) do { unsigned _sp = 0; while (cond) { __builtin_amdgcn_s_sleep(1); \
;     if ((++_sp & 255u) == 0u) { if (xb_ld(&(bar)[XB_TMO])) break; if (_sp > XB_SPIN_CAP) { atomicAdd(&(bar)[XB_TMO], 1u); break; } } } } while (0)
; __device__ __forceinline__ void xcd_barrier(const XcdBarrier& b) {
;     asm volatile("s_waitcnt vmcnt(0)" ::: "memory");
;     __syncthreads();
;     if (threadIdx.x == 0) {
;         unsigned* bar = b.bar;
;         __builtin_amdgcn_s_waitcnt(0);
;         unsigned nloc = b.st[0], nx = b.st[1];
;         if (nloc == 0u) { xcd_barrier_complete(bar, b.x, nloc, nx); b.st[0] = nloc; b.st[1] = nx; }
;         const unsigned old = xb_add(&bar[XB_XSUB(b.x)], 1u);
;         const unsigned gen = old / nloc;
;         if (old + 1u == (gen + 1u) * nloc) {
;             __builtin_amdgcn_fence(__ATOMIC_RELEASE, "agent");
;             asm volatile("s_waitcnt vmcnt(0)" ::: "memory");
;             const unsigned og = xb_add(&bar[XB_TOP], 1u);
;             const unsigned tg = og / nx;
;             if (og + 1u == (tg + 1u) * nx) xb_add(&bar[XB_TOPGEN], 1u);
;             else XB_SPIN(xb_ld(&bar[XB_TOPGEN]) == tg, bar);
;             __builtin_amdgcn_fence(__ATOMIC_ACQUIRE, "agent");
;             xb_add(&bar[XB_XGEN(b.x)], 1u);
;             asm volatile("s_waitcnt vmcnt(0)" ::: "memory");
;         } else {
;             XB_SPIN(xb_ld(&bar[XB_XGEN(b.x)]) == gen, bar);
;             __builtin_amdgcn_fence(__ATOMIC_ACQUIRE, "agent");
;             asm volatile("s_waitcnt vmcnt(0)" ::: "memory");
;         }
;     }
;     __syncthreads();
; }
.Lgh_done_LBB0_1803:
	buffer_inv sc1
	s_waitcnt vmcnt(0)
	v_readlane_b32 s10, v253, 36
	v_readlane_b32 s11, v253, 37
	v_readlane_b32 s14, v253, 55
	s_nop 3
	s_mov_b64 exec, 0xff
	s_add_u32 s12, s10, 0xb000
	s_addc_u32 s13, s11, 0
	s_lshr_b32 s14, s14, 1
	s_add_i32 s14, s14, 1
	s_lshl_b32 s14, s14, 5
	v_mbcnt_lo_u32_b32 v4, -1, 0
	v_lshlrev_b32_e32 v4, 8, v4
	s_mov_b32 s18, 0

; __device__ __forceinline__ void xcd_barrier(const XcdBarrier& b) {
;     ...
;     __syncthreads();
; }
.Lgc_anchor_1803:
	s_branch .LBB0_1803
